# P4: the two per-unit LDS clearing loops (one ds_write_b32 per 8-instruction iteration) replaced by straight-line ds_write2st64_b32 runs
# speedup vs baseline: 1.0086x; 1.0086x over previous
; #define LAS __attribute__((address_space(3)))
; __device__ __forceinline__ int opaque_i(int x) { asm volatile("" : "+v"(x)); return x; }
; __device__ __forceinline__ bool run_unit2(LAS unsigned char* lds, const bf16* y0, const float* aux, unsigned* maskg, int b, int g, int tid_in, int wave, int lane) {
;     const int tid = opaque_i(tid_in);
;     const int lane_o = opaque_i(lane); const int r = lane_o & 31, h2 = lane_o >> 5, t0 = 32 * g;
;     const size_t rowbase = (size_t)b * S;
;     LAS unsigned* hist = (LAS unsigned*)(lds + OFF2_HIST);
;     LAS unsigned* gtm = (LAS unsigned*)(lds + OFF2_GT);
;     for (int i = tid; i < (OFF2_TB) / 4; i += NTHR) ((LAS unsigned*)lds)[i] = 0u;
;     if (tid < 32) { ((LAS unsigned*)(lds + OFF2_CNT))[tid] = 0u; }
;     if (tid == 0) ((LAS int*)(lds + OFF2_FLAG))[0] = 0;
.LBB0_775:
	v_mov_b32_e32 v0, s69
	s_waitcnt lgkmcnt(0)
	s_barrier
	ds_read_b32 v0, v0
	s_waitcnt lgkmcnt(0)
	s_barrier
	v_readfirstlane_b32 s0, v0
	s_cmp_lt_i32 s0, 0
	s_cbranch_scc1 .LBB0_715
	v_mov_b32_e32 v206, v183
	s_movk_i32 s1, 0x6040
	v_mov_b32_e32 v217, v182
	v_cmp_gt_i32_e32 vcc, s1, v206
	s_and_saveexec_b64 s[2:3], vcc
	s_cbranch_execz .LBB0_779
	v_lshl_add_u32 v1, v206, 2, 0
	ds_write2st64_b32 v1, v177, v177 offset0:0 offset1:8
	ds_write2st64_b32 v1, v177, v177 offset0:16 offset1:24
	ds_write2st64_b32 v1, v177, v177 offset0:32 offset1:40
	ds_write2st64_b32 v1, v177, v177 offset0:48 offset1:56
	ds_write2st64_b32 v1, v177, v177 offset0:64 offset1:72
	ds_write2st64_b32 v1, v177, v177 offset0:80 offset1:88
	ds_write2st64_b32 v1, v177, v177 offset0:96 offset1:104
	ds_write2st64_b32 v1, v177, v177 offset0:112 offset1:120
	ds_write2st64_b32 v1, v177, v177 offset0:128 offset1:136
	ds_write2st64_b32 v1, v177, v177 offset0:144 offset1:152
	ds_write2st64_b32 v1, v177, v177 offset0:160 offset1:168
	ds_write2st64_b32 v1, v177, v177 offset0:176 offset1:184
	ds_write2st64_b32 v1, v177, v177 offset0:192 offset1:200
	ds_write2st64_b32 v1, v177, v177 offset0:208 offset1:216
	ds_write2st64_b32 v1, v177, v177 offset0:224 offset1:232
	ds_write2st64_b32 v1, v177, v177 offset0:240 offset1:248
	v_add_u32_e32 v0, 0x10000, v1
	ds_write2st64_b32 v0, v177, v177 offset0:0 offset1:8
	ds_write2st64_b32 v0, v177, v177 offset0:16 offset1:24
	ds_write2st64_b32 v0, v177, v177 offset0:32 offset1:40
	ds_write2st64_b32 v0, v177, v177 offset0:48 offset1:56
	ds_write2st64_b32 v0, v177, v177 offset0:64 offset1:72
	ds_write2st64_b32 v0, v177, v177 offset0:80 offset1:88
	ds_write2st64_b32 v0, v177, v177 offset0:96 offset1:104
	ds_write2st64_b32 v0, v177, v177 offset0:112 offset1:120
	v_cmp_gt_u32_e32 vcc, 64, v206
	s_and_saveexec_b64 s[4:5], vcc
	ds_write_b32 v0, v177 offset:32768
	s_or_b64 exec, exec, s[4:5]
	s_movk_i32 s1, 0x5e3f
	s_mov_b64 s[4:5], exec

; #define LAS __attribute__((address_space(3)))
; __device__ __forceinline__ bool run_unit2(LAS unsigned char* lds, const bf16* y0, const float* aux, unsigned* maskg, int b, int g, int tid_in, int wave, int lane) {
;     ...
;     if (((const LAS int*)(lds + OFF2_FLAG))[0] != 0) { __syncthreads(); return false; }
;     for (int i = tid; i < 65536 / 4; i += NTHR) ((LAS unsigned*)lds)[i] = 0u;
;     __syncthreads();
.LBB0_818:
.LBB0_819:
	s_movk_i32 s0, 0x4000
	v_cmp_gt_i32_e32 vcc, s0, v206
	s_and_saveexec_b64 s[4:5], vcc
	s_cbranch_execz .LBB0_822
	v_lshl_add_u32 v1, v206, 2, 0
	ds_write2st64_b32 v1, v177, v177 offset0:0 offset1:8
	ds_write2st64_b32 v1, v177, v177 offset0:16 offset1:24
	ds_write2st64_b32 v1, v177, v177 offset0:32 offset1:40
	ds_write2st64_b32 v1, v177, v177 offset0:48 offset1:56
	ds_write2st64_b32 v1, v177, v177 offset0:64 offset1:72
	ds_write2st64_b32 v1, v177, v177 offset0:80 offset1:88
	ds_write2st64_b32 v1, v177, v177 offset0:96 offset1:104
	ds_write2st64_b32 v1, v177, v177 offset0:112 offset1:120
	ds_write2st64_b32 v1, v177, v177 offset0:128 offset1:136
	ds_write2st64_b32 v1, v177, v177 offset0:144 offset1:152
	ds_write2st64_b32 v1, v177, v177 offset0:160 offset1:168
	ds_write2st64_b32 v1, v177, v177 offset0:176 offset1:184
	ds_write2st64_b32 v1, v177, v177 offset0:192 offset1:200
	ds_write2st64_b32 v1, v177, v177 offset0:208 offset1:216
	ds_write2st64_b32 v1, v177, v177 offset0:224 offset1:232
	ds_write2st64_b32 v1, v177, v177 offset0:240 offset1:248
	s_movk_i32 s0, 0x3dff
	s_mov_b64 s[6:7], exec
